# v111 without the gate/up loop-head vmcnt(0): the previous unit's output stores now drain behind the next unit's lookup and first loads (signal still issued after the prologue's vmcnt(0)+barrier)
# speedup vs baseline: 1.0070x; 1.0064x over previous
; __device__ __forceinline__ int vwg_id() { const int G = gridDim.x; return (G % 8 == 0) ? (int)((blockIdx.x % 8) * (G / 8) + blockIdx.x / 8) : (int)blockIdx.x; }
; __device__ __forceinline__ bool moe_unit(int cv, int u, int ntiles_n, MoeUnit& mu) {
;     int base = 0;
; #pragma unroll
;     for (int e = 0; e < E; ++e) { const int c = __builtin_amdgcn_readlane(cv, e), tm = (c + 255) >> 8, nu = tm * ntiles_n;
;         if (u < nu) { mu.e = e; mu.cnt = c; mu.base = base; mu.nt = u / tm; mu.mt = u - mu.nt * tm; mu.light = (mu.mt == tm - 1 && c - mu.mt * 256 <= 128) ? 1 : 0; return true; }
;         u -= nu; base += tm * 256; }
;     return false;
; }
; __device__ __forceinline__ void phase_moe_gu(const Ptrs& p, LAS unsigned char* lds) {
;     ...
;     for (int u = vwg_id(); moe_unit(cv, u, 16, mu); u += gridDim.x) {
.LBB0_1006:
	s_lshr_b32 s2, s65, 4
	v_cmp_ge_i32_e32 vcc, s2, v247
	s_bcnt1_i32_b64 s42, vcc
	s_cmp_ge_u32 s42, 32
	s_cbranch_scc1 .LBB0_1288
	s_nop 1
	v_readlane_b32 s87, v1, s42
	v_readlane_b32 s4, v247, s42
	s_add_i32 s3, s87, 0xff
	s_ashr_i32 s3, s3, 8
	s_sub_i32 s4, s4, s3
	s_lshl_b32 s88, s4, 8
	s_lshl_b32 s4, s4, 4
	s_sub_i32 s2, s65, s4
	s_mov_b32 s85, 0
